# MoE GEMM per-tile expert lookup: one lane-parallel LDS read + compare + s_bcnt1 instead of eight dependent LDS reads and ~100 VALU steps
# baseline (speedup 1.0000x reference)
.LBB0_1428:
	s_add_i32 s66, s66, 1
	s_lshl_b32 s21, s66, 5
	v_readlane_b32 s8, v253, 39
	s_add_i32 s21, s21, s8
	v_readlane_b32 s9, v253, 40
	s_cmp_lt_i32 s21, s12
	s_cselect_b64 s[8:9], -1, 0
	s_cmp_ge_i32 s21, s12
	s_cbranch_scc1 .LBB0_1430
	v_mbcnt_lo_u32_b32 v2, -1, 0
	v_mbcnt_hi_u32_b32 v2, -1, v2
	v_lshlrev_b32_e32 v2, 2, v2
	v_add_u32_e32 v2, 0x20400, v2
	ds_read_b32 v2, v2
	s_mov_b32 s42, s21
	s_waitcnt lgkmcnt(0)
	v_cmp_ge_i32_e32 vcc, s21, v2
	s_and_b32 s40, vcc_lo, 0x7fffffff
	s_bcnt1_i32_b32 s40, s40

.LBB0_1502:
	s_add_i32 s60, s60, 1
	s_lshl_b32 s10, s60, 5
	v_readlane_b32 s8, v253, 39
	s_add_i32 s10, s10, s8
	v_readlane_b32 s9, v253, 40
	s_cmp_lt_i32 s10, s2
	s_cselect_b64 s[8:9], -1, 0
	s_cmp_ge_i32 s10, s2
	s_cbranch_scc1 .LBB0_1504
	v_mbcnt_lo_u32_b32 v2, -1, 0
	v_mbcnt_hi_u32_b32 v2, -1, v2
	v_lshlrev_b32_e32 v2, 2, v2
	v_add_u32_e32 v2, 0x20400, v2
	ds_read_b32 v2, v2
	s_mov_b32 s61, s10
	s_waitcnt lgkmcnt(0)
	v_cmp_ge_i32_e32 vcc, s10, v2
	s_and_b32 s40, vcc_lo, 0x7fffffff
	s_bcnt1_i32_b32 s40, s40
